# static s_setprio 1 for waves 4-7 in the dsa, fox and ret attention units
# speedup vs baseline: 1.0115x; 1.0002x over previous
.LBB0_515:
	s_setprio 0
	s_waitcnt lgkmcnt(0)
	s_barrier
	s_and_saveexec_b64 s[0:1], s[36:37]
	s_cbranch_execz .LBB0_517
	s_waitcnt vmcnt(0)
	v_mov_b64_e32 v[4:5], s[6:7]
	global_atomic_add v1, v[4:5], v228, off sc0
	v_mov_b32_e32 v2, s16
	s_waitcnt vmcnt(0) lgkmcnt(0)
	ds_write_b32 v2, v1
.LBB0_517:
	s_or_b64 exec, exec, s[0:1]
	v_mov_b32_e32 v1, s16
	s_waitcnt lgkmcnt(0)
	s_barrier
	ds_read_b32 v1, v1
	s_mov_b64 s[0:1], -1
	s_waitcnt lgkmcnt(0)
	v_cmp_lt_i32_e32 vcc, s75, v1
	v_readfirstlane_b32 s8, v1
	s_cbranch_vccnz .LBB0_514
	s_lshl_b32 s0, s8, 4
	v_mov_b32_e32 v208, v0
	s_and_b32 s19, s0, 0xffffff00
	s_bfe_u32 s10, s8, 0x20002
	v_readfirstlane_b32 s0, v208
	s_bitcmp1_b32 s0, 8
	s_cbranch_scc0 .Lprio_skip_fox
	s_setprio 1
.Lprio_skip_fox:
	s_ashr_i32 s0, s0, 1
	s_and_b32 s11, s8, 3
	s_mov_b32 s1, s88
	v_readlane_b32 s8, v252, 0
	s_andn2_b32 s0, s0, 31
	s_sub_i32 s21, s0, s19
	s_mov_b64 s[8:9], s[68:69]
	s_add_i32 s18, s21, 0xf00
	s_lshl_b32 s17, s11, 7
	s_lshl_b32 s0, s11, 8
	s_add_u32 s12, s8, s0
	s_addc_u32 s13, s9, 0
	s_add_u32 s0, s12, 0x9001000
	s_mul_i32 s14, s10, 0x480
	s_addc_u32 s1, s13, 0
	s_add_i32 s14, s14, s17
	s_mul_i32 s22, s14, 0x2100
	s_add_i32 s22, s22, 0x420000
	s_add_u32 s14, s8, s22
	s_addc_u32 s15, s9, 0
	s_add_u32 s14, s14, 0x2b800000
	v_and_b32_e32 v1, 31, v208
	s_addc_u32 s15, s15, 0
	s_lshl_b32 s20, s10, 16
	s_lshl_b32 s11, s11, 14
	v_or_b32_e32 v211, s18, v1
	s_or_b32 s11, s20, s11
	s_lshl_b32 s23, s10, 12
	s_waitcnt vmcnt(0)
	v_bfe_u32 v5, v208, 5, 1
	v_add_u32_e32 v194, s23, v211
	v_mov_b64_e32 v[6:7], s[0:1]
	s_add_u32 s12, s12, 0x9001400
	v_mad_i64_i32 v[6:7], s[0:1], v194, s24, v[6:7]
	v_lshlrev_b32_e32 v196, 4, v5
	v_mov_b32_e32 v197, v3
	s_addc_u32 s13, s13, 0
	v_lshl_add_u64 v[6:7], v[6:7], 0, v[196:197]
	s_add_u32 s0, s8, s11
	global_load_dwordx4 v[174:177], v[6:7], off
	global_load_dwordx4 v[170:173], v[6:7], off offset:32
	global_load_dwordx4 v[166:169], v[6:7], off offset:64
	global_load_dwordx4 v[162:165], v[6:7], off offset:96
	global_load_dwordx4 v[158:161], v[6:7], off offset:128
	global_load_dwordx4 v[154:157], v[6:7], off offset:160
	global_load_dwordx4 v[150:153], v[6:7], off offset:192
	global_load_dwordx4 v[146:149], v[6:7], off offset:224
	s_addc_u32 s1, s9, 0
	v_ashrrev_i32_e32 v6, 4, v208
	s_add_u32 s10, s0, 0x49200000
	v_add_u32_e32 v2, s23, v6
	v_mov_b64_e32 v[10:11], s[12:13]
	s_addc_u32 s11, s1, 0
	v_mad_i64_i32 v[8:9], s[0:1], v2, s24, v[10:11]
	v_lshlrev_b32_e32 v2, 3, v208
	v_and_b32_e32 v2, 0x78, v2
	v_lshlrev_b32_e32 v2, 1, v2
	v_lshl_add_u64 v[8:9], v[8:9], 0, v[2:3]
	s_waitcnt lgkmcnt(0)
	s_barrier
	global_load_dwordx4 v[12:15], v[8:9], off
	v_add_u32_e32 v9, 0x200, v208
	v_ashrrev_i32_e32 v7, 4, v9
	v_ashrrev_i32_e32 v8, 3, v208
	v_mov_b64_e32 v[24:25], s[14:15]
	s_movk_i32 s14, 0x2100
	v_lshlrev_b32_e32 v28, 4, v208
	v_add_u32_e32 v20, s23, v7
	v_mad_i64_i32 v[16:17], s[0:1], v8, s14, v[24:25]
	v_and_b32_e32 v198, 0x70, v28
	v_mov_b32_e32 v199, v3
	v_mad_i64_i32 v[10:11], s[0:1], v20, s24, v[10:11]
	v_lshl_add_u64 v[16:17], v[16:17], 0, v[198:199]
	v_lshl_add_u64 v[10:11], v[10:11], 0, v[2:3]
	v_ashrrev_i32_e32 v9, 3, v9
	global_load_dwordx4 v[16:19], v[16:17], off
	v_and_b32_e32 v4, 63, v208
	global_load_dwordx4 v[20:23], v[10:11], off
	v_mad_i64_i32 v[10:11], s[0:1], v9, s14, v[24:25]
	v_lshl_add_u64 v[10:11], v[10:11], 0, v[198:199]
	global_load_dwordx4 v[24:27], v[10:11], off
	v_lshlrev_b32_e32 v10, 2, v4
	v_mov_b32_e32 v11, v3
	v_lshl_add_u64 v[10:11], s[10:11], 0, v[10:11]
	global_load_dword v10, v[10:11], off
	s_movk_i32 s25, 0x110
	v_mul_lo_u32 v209, v6, s25
	v_and_b32_e32 v213, 0xf0, v28
	s_movk_i32 s0, 0x88
	v_add3_u32 v11, s72, v209, v213
	v_mul_lo_u32 v214, v8, s0
	s_movk_i32 s1, 0x4400
	v_mul_lo_u32 v215, v7, s25
	v_mul_lo_u32 v216, v9, s0
	s_waitcnt vmcnt(0) lgkmcnt(0)
	ds_write_b128 v11, v[12:15]
	v_add_u32_e32 v11, s72, v214
	v_add3_u32 v11, v11, v198, s1
	ds_write2_b64 v11, v[16:17], v[18:19] offset1:1
	v_add3_u32 v11, s72, v215, v213
	ds_write_b128 v11, v[20:23]
	v_add_u32_e32 v11, s72, v216
	v_add3_u32 v11, v11, v198, s1
	v_cmp_gt_i32_e64 s[0:1], 64, v208
	ds_write2_b64 v11, v[24:25], v[26:27] offset1:1
	s_and_saveexec_b64 s[14:15], s[0:1]
	v_mul_f32_e32 v10, 0x3fb8aa3b, v10
	v_lshl_add_u32 v11, v208, 2, s72
	ds_write_b32 v11, v10 offset:34816
	s_or_b64 exec, exec, s[14:15]
	s_movk_i32 s20, 0x2100
	v_mad_i64_i32 v[10:11], s[14:15], v8, s20, 0
	v_mad_i64_i32 v[8:9], s[14:15], v9, s20, 0
	s_sub_i32 s14, 0x1000, s19
	s_lshr_b32 s15, s14, 6
	s_add_i32 s19, s21, 0xf1f
	v_lshl_add_u64 v[200:201], s[12:13], 0, v[2:3]
	s_add_u32 s12, s8, s22
	v_and_b32_e32 v2, 7, v208
	s_addc_u32 s13, s9, 0
	v_lshlrev_b32_e32 v2, 4, v2
	s_add_u32 s12, s12, 0x2b800080
	v_lshlrev_b32_e32 v197, 3, v5
	v_mul_u32_u24_e32 v217, 0x110, v1
	v_mul_u32_u24_e32 v199, 0x88, v1
	v_lshlrev_b32_e32 v1, 2, v5
	v_or_b32_e32 v218, 64, v4
	v_lshl_add_u64 v[4:5], v[8:9], 0, v[2:3]
	s_addc_u32 s13, s13, 0
	v_lshl_add_u64 v[202:203], s[12:13], 0, v[4:5]
	v_lshl_add_u64 v[4:5], v[10:11], 0, v[2:3]
	v_mov_b32_e32 v16, v3
	v_mov_b32_e32 v17, v3
	v_add3_u32 v219, v7, s23, 64
	v_add3_u32 v220, v6, s23, 64
	v_lshl_add_u64 v[204:205], s[12:13], 0, v[4:5]
	v_mov_b32_e32 v2, v3
	v_mov_b32_e32 v4, v3
	v_mov_b32_e32 v5, v3
	v_mov_b32_e32 v6, v3
	v_mov_b32_e32 v7, v3
	v_mov_b32_e32 v8, v3
	v_mov_b32_e32 v9, v3
	v_mov_b32_e32 v10, v3
	v_mov_b32_e32 v11, v3
	v_mov_b32_e32 v12, v3
	v_mov_b32_e32 v13, v3
	v_mov_b32_e32 v14, v3
	v_mov_b32_e32 v15, v3
	v_mov_b64_e32 v[32:33], v[16:17]
	v_mov_b64_e32 v[48:49], v[16:17]
	v_mov_b64_e32 v[64:65], v[16:17]
	v_mov_b64_e32 v[80:81], v[16:17]
	v_ashrrev_i32_e32 v195, 31, v194
	s_mov_b32 s20, 1
	s_mov_b32 s14, 0
	v_mov_b32_e32 v212, 0xf149f2ca
	v_mov_b32_e32 v210, 0
	v_mov_b64_e32 v[30:31], v[14:15]
	v_mov_b64_e32 v[28:29], v[12:13]
	v_mov_b64_e32 v[26:27], v[10:11]
	v_mov_b64_e32 v[24:25], v[8:9]
	v_mov_b64_e32 v[22:23], v[6:7]
	v_mov_b64_e32 v[20:21], v[4:5]
	v_mov_b64_e32 v[18:19], v[2:3]
	v_mov_b64_e32 v[46:47], v[14:15]
	v_mov_b64_e32 v[44:45], v[12:13]
	v_mov_b64_e32 v[42:43], v[10:11]
	v_mov_b64_e32 v[40:41], v[8:9]
	v_mov_b64_e32 v[38:39], v[6:7]
	v_mov_b64_e32 v[36:37], v[4:5]
	v_mov_b64_e32 v[34:35], v[2:3]
	v_mov_b64_e32 v[62:63], v[14:15]
	v_mov_b64_e32 v[60:61], v[12:13]
	v_mov_b64_e32 v[58:59], v[10:11]
	v_mov_b64_e32 v[56:57], v[8:9]
	v_mov_b64_e32 v[54:55], v[6:7]
	v_mov_b64_e32 v[52:53], v[4:5]
	v_mov_b64_e32 v[50:51], v[2:3]
	v_mov_b64_e32 v[78:79], v[14:15]
	v_mov_b64_e32 v[76:77], v[12:13]
	v_mov_b64_e32 v[74:75], v[10:11]
	v_mov_b64_e32 v[72:73], v[8:9]
	v_mov_b64_e32 v[70:71], v[6:7]
	v_mov_b64_e32 v[68:69], v[4:5]
	v_mov_b64_e32 v[66:67], v[2:3]
	s_mov_b32 s25, 0x800000
	s_movk_i32 s24, 0x7200
	s_waitcnt lgkmcnt(0)
	s_barrier
	s_branch .LBB0_522

.LBB0_1136:
	s_setprio 0
	s_waitcnt vmcnt(0) lgkmcnt(0)
	s_barrier
	s_and_saveexec_b64 s[2:3], s[36:37]
	s_cbranch_execz .LBB0_1138
	v_mov_b64_e32 v[4:5], s[0:1]
	global_atomic_add v1, v[4:5], v228, off sc0
	v_mov_b32_e32 v2, s10
	s_waitcnt vmcnt(0) lgkmcnt(0)
	ds_write_b32 v2, v1
.LBB0_1138:
	s_or_b64 exec, exec, s[2:3]
	v_mov_b32_e32 v1, s10
	s_waitcnt lgkmcnt(0)
	s_barrier
	ds_read_b32 v1, v1
	s_mov_b64 s[2:3], -1
	s_waitcnt lgkmcnt(0)
	v_cmp_lt_i32_e32 vcc, s75, v1
	v_readfirstlane_b32 s4, v1
	s_cbranch_vccnz .LBB0_1135
	v_mov_b32_e32 v209, v0
	s_lshl_b32 s2, s4, 4
	s_bfe_u32 s14, s4, 0x20002
	v_readfirstlane_b32 s8, v209
	s_bitcmp1_b32 s8, 8
	s_cbranch_scc0 .Lprio_skip_ret
	s_setprio 1
.Lprio_skip_ret:
	s_and_b32 s15, s4, 3
	s_and_b32 s4, s2, 0xffffff00
	v_readlane_b32 s2, v252, 0
	s_mov_b32 s3, s88
	s_ashr_i32 s5, s8, 1
	s_and_b32 s16, s5, 0xffffffe0
	s_mov_b64 s[2:3], s[68:69]
	s_add_i32 s16, s16, s4
	s_lshl_b32 s5, s15, 7
	s_lshl_b32 s6, s15, 8
	v_and_b32_e32 v4, 31, v209
	s_add_u32 s6, s2, s6
	v_or_b32_e32 v207, s16, v4
	s_addc_u32 s7, s3, 0
	s_lshl_b32 s9, s14, 12
	v_add_u32_e32 v180, s9, v207
	v_ashrrev_i32_e32 v181, 31, v180
	v_bfe_u32 v5, v209, 5, 1
	v_lshlrev_b64 v[6:7], 10, v[180:181]
	v_lshl_add_u64 v[6:7], s[6:7], 0, v[6:7]
	v_lshlrev_b32_e32 v2, 4, v5
	v_lshl_add_u64 v[6:7], v[6:7], 0, v[2:3]
	s_mov_b64 s[6:7], 0x29800000
	v_lshl_add_u64 v[8:9], v[6:7], 0, s[6:7]
	s_mov_b32 s6, 0x29800000
	v_add_co_u32_e32 v6, vcc, s6, v6
	v_cvt_f32_ubyte0_e32 v1, s15
	s_nop 0
	v_addc_co_u32_e32 v7, vcc, 0, v7, vcc
	global_load_dwordx4 v[124:127], v[8:9], off offset:32
	global_load_dwordx4 v[120:123], v[8:9], off offset:64
	global_load_dwordx4 v[116:119], v[8:9], off offset:96
	global_load_dwordx4 v[112:115], v[8:9], off offset:128
	global_load_dwordx4 v[108:111], v[8:9], off offset:160
	global_load_dwordx4 v[104:107], v[8:9], off offset:192
	global_load_dwordx4 v[128:131], v[6:7], off
	global_load_dwordx4 v[100:103], v[8:9], off offset:224
	v_sub_f32_e32 v1, 0xc0a00000, v1
	s_mov_b32 s6, 0xc2fc0000
	v_cmp_gt_f32_e32 vcc, s6, v1
	v_mov_b32_e32 v6, 0x42800000
	s_and_b64 s[6:7], vcc, exec
	v_cndmask_b32_e32 v6, 0, v6, vcc
	v_add_f32_e32 v1, v1, v6
	v_exp_f32_e32 v1, v1
	s_cselect_b32 s6, 0xffffffc0, 0
	v_mov_b32_e32 v6, 0x42000000
	s_waitcnt lgkmcnt(0)
	v_ldexp_f32 v1, v1, s6
	v_sub_f32_e32 v1, 1.0, v1
	v_cmp_gt_f32_e32 vcc, s25, v1
	s_and_b64 s[6:7], vcc, exec
	s_cselect_b32 s6, 32, 0
	v_ldexp_f32 v1, v1, s6
	v_log_f32_e32 v1, v1
	v_cndmask_b32_e32 v6, 0, v6, vcc
	v_cmp_gt_i32_e32 vcc, 64, v209
	s_barrier
	v_sub_f32_e32 v208, v1, v6
	s_and_saveexec_b64 s[6:7], vcc
	s_cbranch_execz .LBB0_1141
	v_sub_u32_e32 v1, 63, v209
	v_cvt_f32_u32_e32 v1, v1
	s_mov_b32 s13, 0xc2fc0000
	v_not_b32_e32 v7, 63
	v_mul_f32_e32 v6, v208, v1
	v_cmp_gt_f32_e32 vcc, s13, v6
	v_mov_b32_e32 v6, 0x42800000
	s_nop 0
	v_cndmask_b32_e32 v6, 0, v6, vcc
	v_fmac_f32_e32 v6, v208, v1
	v_exp_f32_e32 v1, v6
	v_cndmask_b32_e32 v7, 0, v7, vcc
	v_lshl_add_u32 v6, v209, 2, s11
	v_ldexp_f32 v1, v1, v7
	ds_write_b32 v6, v1

.LBB0_1211:
	s_setprio 0
	s_waitcnt vmcnt(0) lgkmcnt(0)
	s_barrier
	s_and_saveexec_b64 s[0:1], s[36:37]
	s_cbranch_execz .LBB0_1213
	v_mov_b64_e32 v[4:5], s[6:7]
	global_atomic_add v1, v[4:5], v228, off sc0
	v_mov_b32_e32 v2, s16
	s_waitcnt vmcnt(0) lgkmcnt(0)
	ds_write_b32 v2, v1
.LBB0_1213:
	s_or_b64 exec, exec, s[0:1]
	v_mov_b32_e32 v1, s16
	s_waitcnt lgkmcnt(0)
	s_barrier
	ds_read_b32 v1, v1
	s_mov_b64 s[0:1], -1
	s_waitcnt lgkmcnt(0)
	v_cmp_lt_i32_e32 vcc, s75, v1
	v_readfirstlane_b32 s8, v1
	s_cbranch_vccnz .LBB0_1210
	v_mov_b32_e32 v4, v0
	v_readlane_b32 s0, v252, 0
	s_mov_b32 s1, s88
	s_lshl_b32 s20, s8, 4
	v_readfirstlane_b32 s21, v4
	s_bitcmp1_b32 s21, 8
	s_cbranch_scc0 .Lprio_skip_dsa
	s_setprio 1
.Lprio_skip_dsa:
	s_lshr_b32 s0, s21, 1
	s_andn2_b32 s20, s20, 63
	s_and_b32 s0, s0, 32
	s_and_b32 s10, s21, 0xffffff80
	s_sub_i32 s14, s0, s20
	s_ashr_i32 s11, s10, 31
	s_and_b32 s18, s8, 3
	s_mov_b64 s[8:9], s[68:69]
	s_add_i32 s15, s14, 0xfc0
	s_lshl_b64 s[0:1], s[10:11], 1
	s_add_u32 s0, s8, s0
	s_addc_u32 s1, s9, s1
	v_and_b32_e32 v8, 31, v4
	s_add_u32 s0, s0, 0x2de00000
	v_or_b32_e32 v1, s15, v8
	s_addc_u32 s1, s1, 0
	s_lshl_b32 s19, s18, 12
	v_bfe_u32 v9, v4, 5, 1
	v_add_u32_e32 v2, s19, v1
	v_mov_b64_e32 v[6:7], s[0:1]
	s_movk_i32 s0, 0xc00
	v_mad_u64_u32 v[6:7], s[0:1], v2, s0, v[6:7]
	v_lshlrev_b32_e32 v148, 4, v9
	v_mov_b32_e32 v149, v3
	v_lshl_add_u64 v[6:7], v[6:7], 0, v[148:149]
	global_load_dwordx4 v[100:103], v[6:7], off
	global_load_dwordx4 v[104:107], v[6:7], off offset:32
	global_load_dwordx4 v[108:111], v[6:7], off offset:64
	global_load_dwordx4 v[112:115], v[6:7], off offset:96
	global_load_dwordx4 v[116:119], v[6:7], off offset:128
	global_load_dwordx4 v[120:123], v[6:7], off offset:160
	global_load_dwordx4 v[124:127], v[6:7], off offset:192
	global_load_dwordx4 v[128:131], v[6:7], off offset:224
	v_lshl_add_u64 v[6:7], v[2:3], 2, s[8:9]
	v_add_co_u32_e32 v6, vcc, 0x49240000, v6
	s_movk_i32 s0, 0x204
	s_nop 0
	v_addc_co_u32_e32 v7, vcc, 0, v7, vcc
	global_load_dword v10, v[6:7], off
	v_cmp_gt_i32_e32 vcc, s0, v4
	s_waitcnt lgkmcnt(0)
	s_barrier
	s_and_saveexec_b64 s[0:1], vcc
	s_cbranch_execz .LBB0_1217
	v_ashrrev_i32_e32 v5, 31, v4
	v_lshl_add_u64 v[6:7], v[4:5], 2, s[8:9]
	s_mov_b64 s[12:13], 0x300000
	v_add_u32_e32 v1, 0xfffffe00, v4
	v_lshl_add_u32 v11, v4, 2, s17
	v_lshl_add_u64 v[6:7], v[6:7], 0, s[12:13]
	s_mov_b64 s[12:13], 0
